# removed per-phase s_setprio flips in the in-projection GEMM K-loop (A/B of the priority flips), on top of prep-loop rewrite + new conversion queue
# speedup vs baseline: 1.0000x; 1.0000x over previous
.LBB0_85:
	ds_read_b128 v[154:157], v150
	ds_read_b128 v[158:161], v150 offset:1024
	ds_read_b128 v[162:165], v150 offset:2048
	ds_read_b128 v[166:169], v150 offset:3072
	s_add_u32 s60, s24, 0xfff80080
	s_addc_u32 s61, s25, -1
	s_cmp_eq_u32 s59, 28
	s_cselect_b32 s87, s15, s61
	s_cselect_b32 s86, s55, s60
	s_cselect_b32 s85, s13, s58
	s_cselect_b32 s84, s56, s57
	v_lshl_add_u64 v[202:203], s[24:25], 0, v[138:139]
	s_add_i32 m0, s11, 0xc000
	ds_read_b128 v[170:173], v151
	ds_read_b128 v[174:177], v151 offset:1024
	ds_read_b128 v[178:181], v151 offset:2048
	ds_read_b128 v[182:185], v151 offset:3072
	ds_read_b128 v[186:189], v151 offset:4096
	ds_read_b128 v[190:193], v151 offset:5120
	ds_read_b128 v[194:197], v151 offset:6144
	ds_read_b128 v[198:201], v151 offset:7168
	global_load_lds_dwordx4 v[202:203], off
	v_lshl_add_u64 v[202:203], s[24:25], 0, v[140:141]
	s_add_i32 m0, s11, 0xe000
	s_nop 0
	global_load_lds_dwordx4 v[202:203], off
	s_waitcnt lgkmcnt(8)
	s_barrier
	s_waitcnt lgkmcnt(0)
	s_waitcnt lgkmcnt(0)
	v_mfma_f32_16x16x32_bf16 v[126:129], v[154:157], v[170:173], v[126:129]
	v_mfma_f32_16x16x32_bf16 v[122:125], v[162:165], v[170:173], v[122:125]
	v_mfma_f32_16x16x32_bf16 v[118:121], v[154:157], v[178:181], v[118:121]
	v_mfma_f32_16x16x32_bf16 v[114:117], v[162:165], v[178:181], v[114:117]
	v_mfma_f32_16x16x32_bf16 v[102:105], v[154:157], v[186:189], v[102:105]
	v_mfma_f32_16x16x32_bf16 v[98:101], v[162:165], v[186:189], v[98:101]
	v_mfma_f32_16x16x32_bf16 v[86:89], v[154:157], v[194:197], v[86:89]
	v_mfma_f32_16x16x32_bf16 v[82:85], v[162:165], v[194:197], v[82:85]
	v_mfma_f32_16x16x32_bf16 v[126:129], v[158:161], v[174:177], v[126:129]
	v_mfma_f32_16x16x32_bf16 v[122:125], v[166:169], v[174:177], v[122:125]
	v_mfma_f32_16x16x32_bf16 v[118:121], v[158:161], v[182:185], v[118:121]
	v_mfma_f32_16x16x32_bf16 v[114:117], v[166:169], v[182:185], v[114:117]
	v_mfma_f32_16x16x32_bf16 v[102:105], v[158:161], v[190:193], v[102:105]
	v_mfma_f32_16x16x32_bf16 v[98:101], v[166:169], v[190:193], v[98:101]
	v_mfma_f32_16x16x32_bf16 v[86:89], v[158:161], v[198:201], v[86:89]
	v_mfma_f32_16x16x32_bf16 v[82:85], v[166:169], v[198:201], v[82:85]
	s_barrier
	s_add_i32 s60, s41, s18
	v_lshl_add_u64 v[218:219], s[84:85], 0, v[134:135]
	s_mov_b32 m0, s60
	ds_read_b128 v[202:205], v152
	ds_read_b128 v[206:209], v152 offset:1024
	ds_read_b128 v[210:213], v152 offset:2048
	ds_read_b128 v[214:217], v152 offset:3072
	global_load_lds_dwordx4 v[218:219], off
	v_lshl_add_u64 v[220:221], s[84:85], 0, v[130:131]
	s_add_i32 m0, s60, 0x2000
	s_nop 0
	global_load_lds_dwordx4 v[220:221], off
	s_barrier
	s_waitcnt lgkmcnt(0)
	s_waitcnt lgkmcnt(0)
	v_mfma_f32_16x16x32_bf16 v[110:113], v[202:205], v[170:173], v[110:113]
	v_mfma_f32_16x16x32_bf16 v[106:109], v[210:213], v[170:173], v[106:109]
	v_mfma_f32_16x16x32_bf16 v[94:97], v[202:205], v[178:181], v[94:97]
	v_mfma_f32_16x16x32_bf16 v[90:93], v[210:213], v[178:181], v[90:93]
	v_mfma_f32_16x16x32_bf16 v[78:81], v[202:205], v[186:189], v[78:81]
	v_mfma_f32_16x16x32_bf16 v[74:77], v[210:213], v[186:189], v[74:77]
	v_mfma_f32_16x16x32_bf16 v[70:73], v[202:205], v[194:197], v[70:73]
	v_mfma_f32_16x16x32_bf16 v[66:69], v[210:213], v[194:197], v[66:69]
	v_mfma_f32_16x16x32_bf16 v[110:113], v[206:209], v[174:177], v[110:113]
	v_mfma_f32_16x16x32_bf16 v[106:109], v[214:217], v[174:177], v[106:109]
	v_mfma_f32_16x16x32_bf16 v[94:97], v[206:209], v[182:185], v[94:97]
	v_mfma_f32_16x16x32_bf16 v[90:93], v[214:217], v[182:185], v[90:93]
	v_mfma_f32_16x16x32_bf16 v[78:81], v[206:209], v[190:193], v[78:81]
	v_mfma_f32_16x16x32_bf16 v[74:77], v[214:217], v[190:193], v[74:77]
	v_mfma_f32_16x16x32_bf16 v[70:73], v[206:209], v[198:201], v[70:73]
	v_mfma_f32_16x16x32_bf16 v[66:69], v[214:217], v[198:201], v[66:69]
	s_mov_b32 m0, s11
	v_lshl_add_u64 v[222:223], s[86:87], 0, v[136:137]
	s_barrier
	ds_read_b128 v[170:173], v151 offset:16384
	ds_read_b128 v[174:177], v151 offset:17408
	ds_read_b128 v[178:181], v151 offset:18432
	ds_read_b128 v[182:185], v151 offset:19456
	ds_read_b128 v[186:189], v151 offset:20480
	ds_read_b128 v[190:193], v151 offset:21504
	ds_read_b128 v[194:197], v151 offset:22528
	ds_read_b128 v[198:201], v151 offset:23552
	global_load_lds_dwordx4 v[222:223], off
	v_lshl_add_u64 v[224:225], s[86:87], 0, v[132:133]
	s_mov_b32 m0, s21
	s_nop 0
	global_load_lds_dwordx4 v[224:225], off
	s_barrier
	s_waitcnt lgkmcnt(0)
	s_waitcnt lgkmcnt(0)
	v_mfma_f32_16x16x32_bf16 v[62:65], v[154:157], v[170:173], v[62:65]
	v_mfma_f32_16x16x32_bf16 v[58:61], v[162:165], v[170:173], v[58:61]
	v_mfma_f32_16x16x32_bf16 v[54:57], v[154:157], v[178:181], v[54:57]
	v_mfma_f32_16x16x32_bf16 v[50:53], v[162:165], v[178:181], v[50:53]
	v_mfma_f32_16x16x32_bf16 v[38:41], v[154:157], v[186:189], v[38:41]
	v_mfma_f32_16x16x32_bf16 v[34:37], v[162:165], v[186:189], v[34:37]
	v_mfma_f32_16x16x32_bf16 v[22:25], v[154:157], v[194:197], v[22:25]
	v_mfma_f32_16x16x32_bf16 v[18:21], v[162:165], v[194:197], v[18:21]
	v_mfma_f32_16x16x32_bf16 v[62:65], v[158:161], v[174:177], v[62:65]
	v_mfma_f32_16x16x32_bf16 v[58:61], v[166:169], v[174:177], v[58:61]
	v_mfma_f32_16x16x32_bf16 v[54:57], v[158:161], v[182:185], v[54:57]
	v_mfma_f32_16x16x32_bf16 v[50:53], v[166:169], v[182:185], v[50:53]
	v_mfma_f32_16x16x32_bf16 v[38:41], v[158:161], v[190:193], v[38:41]
	v_mfma_f32_16x16x32_bf16 v[34:37], v[166:169], v[190:193], v[34:37]
	v_mfma_f32_16x16x32_bf16 v[22:25], v[158:161], v[198:201], v[22:25]
	v_mfma_f32_16x16x32_bf16 v[18:21], v[166:169], v[198:201], v[18:21]
	s_barrier
	s_add_u32 s60, s84, 0x80000
	s_addc_u32 s61, s85, 0
	s_add_i32 s62, s52, s18
	v_lshl_add_u64 v[154:155], s[60:61], 0, v[134:135]
	s_mov_b32 m0, s62
	s_nop 0
	global_load_lds_dwordx4 v[154:155], off
	v_lshl_add_u64 v[154:155], s[60:61], 0, v[130:131]
	s_add_i32 m0, s62, 0x2000
	s_nop 0
	global_load_lds_dwordx4 v[154:155], off
	s_waitcnt vmcnt(6)
	s_barrier
	v_mfma_f32_16x16x32_bf16 v[46:49], v[202:205], v[170:173], v[46:49]
	v_mfma_f32_16x16x32_bf16 v[42:45], v[210:213], v[170:173], v[42:45]
	v_mfma_f32_16x16x32_bf16 v[30:33], v[202:205], v[178:181], v[30:33]
	v_mfma_f32_16x16x32_bf16 v[26:29], v[210:213], v[178:181], v[26:29]
	v_mfma_f32_16x16x32_bf16 v[14:17], v[202:205], v[186:189], v[14:17]
	v_mfma_f32_16x16x32_bf16 v[10:13], v[210:213], v[186:189], v[10:13]
	v_mfma_f32_16x16x32_bf16 v[6:9], v[202:205], v[194:197], v[6:9]
	v_mfma_f32_16x16x32_bf16 v[2:5], v[210:213], v[194:197], v[2:5]
	v_mfma_f32_16x16x32_bf16 v[46:49], v[206:209], v[174:177], v[46:49]
	v_mfma_f32_16x16x32_bf16 v[42:45], v[214:217], v[174:177], v[42:45]
	v_mfma_f32_16x16x32_bf16 v[30:33], v[206:209], v[182:185], v[30:33]
	v_mfma_f32_16x16x32_bf16 v[26:29], v[214:217], v[182:185], v[26:29]
	v_mfma_f32_16x16x32_bf16 v[14:17], v[206:209], v[190:193], v[14:17]
	v_mfma_f32_16x16x32_bf16 v[10:13], v[214:217], v[190:193], v[10:13]
	v_mfma_f32_16x16x32_bf16 v[6:9], v[206:209], v[198:201], v[6:9]
	v_mfma_f32_16x16x32_bf16 v[2:5], v[214:217], v[198:201], v[2:5]
	s_add_i32 s62, 0, 0x18000
	v_add_u32_e32 v1, s62, v148
	s_barrier
	ds_read_b128 v[154:157], v1
	ds_read_b128 v[158:161], v1 offset:1024
	ds_read_b128 v[162:165], v1 offset:2048
	ds_read_b128 v[166:169], v1 offset:3072
	s_add_u32 s60, s86, 0x80000
	s_addc_u32 s61, s87, 0
	s_mov_b32 m0, s26
	v_lshl_add_u64 v[202:203], s[60:61], 0, v[136:137]
	ds_read_b128 v[170:173], v151 offset:32768
	ds_read_b128 v[174:177], v151 offset:33792
	ds_read_b128 v[178:181], v151 offset:34816
	ds_read_b128 v[182:185], v151 offset:35840
	ds_read_b128 v[186:189], v151 offset:36864
	ds_read_b128 v[190:193], v151 offset:37888
	ds_read_b128 v[194:197], v151 offset:38912
	ds_read_b128 v[198:201], v151 offset:39936
	global_load_lds_dwordx4 v[202:203], off
	v_lshl_add_u64 v[202:203], s[60:61], 0, v[132:133]
	s_mov_b32 m0, s27
	s_nop 0
	global_load_lds_dwordx4 v[202:203], off
	s_waitcnt lgkmcnt(8)
	s_barrier
	s_waitcnt lgkmcnt(0)
	s_waitcnt lgkmcnt(0)
	v_mfma_f32_16x16x32_bf16 v[126:129], v[154:157], v[170:173], v[126:129]
	v_mfma_f32_16x16x32_bf16 v[122:125], v[162:165], v[170:173], v[122:125]
	v_mfma_f32_16x16x32_bf16 v[118:121], v[154:157], v[178:181], v[118:121]
	v_mfma_f32_16x16x32_bf16 v[114:117], v[162:165], v[178:181], v[114:117]
	v_mfma_f32_16x16x32_bf16 v[102:105], v[154:157], v[186:189], v[102:105]
	v_mfma_f32_16x16x32_bf16 v[98:101], v[162:165], v[186:189], v[98:101]
	v_mfma_f32_16x16x32_bf16 v[86:89], v[154:157], v[194:197], v[86:89]
	v_mfma_f32_16x16x32_bf16 v[82:85], v[162:165], v[194:197], v[82:85]
	v_mfma_f32_16x16x32_bf16 v[126:129], v[158:161], v[174:177], v[126:129]
	v_mfma_f32_16x16x32_bf16 v[122:125], v[166:169], v[174:177], v[122:125]
	v_mfma_f32_16x16x32_bf16 v[118:121], v[158:161], v[182:185], v[118:121]
	v_mfma_f32_16x16x32_bf16 v[114:117], v[166:169], v[182:185], v[114:117]
	v_mfma_f32_16x16x32_bf16 v[102:105], v[158:161], v[190:193], v[102:105]
	v_mfma_f32_16x16x32_bf16 v[98:101], v[166:169], v[190:193], v[98:101]
	v_mfma_f32_16x16x32_bf16 v[86:89], v[158:161], v[198:201], v[86:89]
	v_mfma_f32_16x16x32_bf16 v[82:85], v[166:169], v[198:201], v[82:85]
	s_barrier
	s_add_i32 s63, 0, 0x1c000
	s_add_i32 s60, s62, s18
	v_add_u32_e32 v1, s63, v148
	v_lshl_add_u64 v[218:219], v[218:219], 0, s[8:9]
	s_mov_b32 m0, s60
	ds_read_b128 v[202:205], v1
	ds_read_b128 v[206:209], v1 offset:1024
	ds_read_b128 v[210:213], v1 offset:2048
	ds_read_b128 v[214:217], v1 offset:3072
	global_load_lds_dwordx4 v[218:219], off
	v_lshl_add_u64 v[218:219], v[220:221], 0, s[8:9]
	s_add_i32 m0, s60, 0x2000
	s_nop 0
	global_load_lds_dwordx4 v[218:219], off
	s_barrier
	s_waitcnt lgkmcnt(0)
	s_waitcnt lgkmcnt(0)
	v_mfma_f32_16x16x32_bf16 v[110:113], v[202:205], v[170:173], v[110:113]
	v_mfma_f32_16x16x32_bf16 v[106:109], v[210:213], v[170:173], v[106:109]
	v_mfma_f32_16x16x32_bf16 v[94:97], v[202:205], v[178:181], v[94:97]
	v_mfma_f32_16x16x32_bf16 v[90:93], v[210:213], v[178:181], v[90:93]
	v_mfma_f32_16x16x32_bf16 v[78:81], v[202:205], v[186:189], v[78:81]
	v_mfma_f32_16x16x32_bf16 v[74:77], v[210:213], v[186:189], v[74:77]
	v_mfma_f32_16x16x32_bf16 v[70:73], v[202:205], v[194:197], v[70:73]
	v_mfma_f32_16x16x32_bf16 v[66:69], v[210:213], v[194:197], v[66:69]
	v_mfma_f32_16x16x32_bf16 v[110:113], v[206:209], v[174:177], v[110:113]
	v_mfma_f32_16x16x32_bf16 v[106:109], v[214:217], v[174:177], v[106:109]
	v_mfma_f32_16x16x32_bf16 v[94:97], v[206:209], v[182:185], v[94:97]
	v_mfma_f32_16x16x32_bf16 v[90:93], v[214:217], v[182:185], v[90:93]
	v_mfma_f32_16x16x32_bf16 v[78:81], v[206:209], v[190:193], v[78:81]
	v_mfma_f32_16x16x32_bf16 v[74:77], v[214:217], v[190:193], v[74:77]
	v_mfma_f32_16x16x32_bf16 v[70:73], v[206:209], v[198:201], v[70:73]
	v_mfma_f32_16x16x32_bf16 v[66:69], v[214:217], v[198:201], v[66:69]
	s_mov_b32 m0, s34
	v_lshl_add_u64 v[218:219], v[222:223], 0, s[8:9]
	s_barrier
	ds_read_b128 v[170:173], v151 offset:49152
	ds_read_b128 v[174:177], v151 offset:50176
	ds_read_b128 v[178:181], v151 offset:51200
	ds_read_b128 v[182:185], v151 offset:52224
	ds_read_b128 v[186:189], v151 offset:53248
	ds_read_b128 v[190:193], v151 offset:54272
	ds_read_b128 v[194:197], v151 offset:55296
	ds_read_b128 v[198:201], v151 offset:56320
	global_load_lds_dwordx4 v[218:219], off
	v_lshl_add_u64 v[218:219], v[224:225], 0, s[8:9]
	s_mov_b32 m0, s35
	s_nop 0
	global_load_lds_dwordx4 v[218:219], off
	s_barrier
	s_waitcnt lgkmcnt(0)
	s_waitcnt lgkmcnt(0)
	v_mfma_f32_16x16x32_bf16 v[62:65], v[154:157], v[170:173], v[62:65]
	v_mfma_f32_16x16x32_bf16 v[58:61], v[162:165], v[170:173], v[58:61]
	v_mfma_f32_16x16x32_bf16 v[54:57], v[154:157], v[178:181], v[54:57]
	v_mfma_f32_16x16x32_bf16 v[50:53], v[162:165], v[178:181], v[50:53]
	v_mfma_f32_16x16x32_bf16 v[38:41], v[154:157], v[186:189], v[38:41]
	v_mfma_f32_16x16x32_bf16 v[34:37], v[162:165], v[186:189], v[34:37]
	v_mfma_f32_16x16x32_bf16 v[22:25], v[154:157], v[194:197], v[22:25]
	v_mfma_f32_16x16x32_bf16 v[18:21], v[162:165], v[194:197], v[18:21]
	v_mfma_f32_16x16x32_bf16 v[62:65], v[158:161], v[174:177], v[62:65]
	v_mfma_f32_16x16x32_bf16 v[58:61], v[166:169], v[174:177], v[58:61]
	v_mfma_f32_16x16x32_bf16 v[54:57], v[158:161], v[182:185], v[54:57]
	v_mfma_f32_16x16x32_bf16 v[50:53], v[166:169], v[182:185], v[50:53]
	v_mfma_f32_16x16x32_bf16 v[38:41], v[158:161], v[190:193], v[38:41]
	v_mfma_f32_16x16x32_bf16 v[34:37], v[166:169], v[190:193], v[34:37]
	v_mfma_f32_16x16x32_bf16 v[22:25], v[158:161], v[198:201], v[22:25]
	v_mfma_f32_16x16x32_bf16 v[18:21], v[166:169], v[198:201], v[18:21]
	s_barrier
	s_add_u32 s60, s84, 0x80080
	s_addc_u32 s61, s85, 0
	s_add_i32 s62, s63, s18
	v_lshl_add_u64 v[154:155], s[60:61], 0, v[134:135]
	s_mov_b32 m0, s62
	s_nop 0
	global_load_lds_dwordx4 v[154:155], off
	v_lshl_add_u64 v[154:155], s[60:61], 0, v[130:131]
	s_add_i32 m0, s62, 0x2000
	s_nop 0
	global_load_lds_dwordx4 v[154:155], off
	s_waitcnt vmcnt(6)
	s_barrier
	v_mfma_f32_16x16x32_bf16 v[46:49], v[202:205], v[170:173], v[46:49]
	v_mfma_f32_16x16x32_bf16 v[42:45], v[210:213], v[170:173], v[42:45]
	v_mfma_f32_16x16x32_bf16 v[30:33], v[202:205], v[178:181], v[30:33]
	v_mfma_f32_16x16x32_bf16 v[26:29], v[210:213], v[178:181], v[26:29]
	v_mfma_f32_16x16x32_bf16 v[14:17], v[202:205], v[186:189], v[14:17]
	v_mfma_f32_16x16x32_bf16 v[10:13], v[210:213], v[186:189], v[10:13]
	v_mfma_f32_16x16x32_bf16 v[6:9], v[202:205], v[194:197], v[6:9]
	v_mfma_f32_16x16x32_bf16 v[2:5], v[210:213], v[194:197], v[2:5]
	v_mfma_f32_16x16x32_bf16 v[46:49], v[206:209], v[174:177], v[46:49]
	v_mfma_f32_16x16x32_bf16 v[42:45], v[214:217], v[174:177], v[42:45]
	v_mfma_f32_16x16x32_bf16 v[30:33], v[206:209], v[182:185], v[30:33]
	v_mfma_f32_16x16x32_bf16 v[26:29], v[214:217], v[182:185], v[26:29]
	v_mfma_f32_16x16x32_bf16 v[14:17], v[206:209], v[190:193], v[14:17]
	v_mfma_f32_16x16x32_bf16 v[10:13], v[214:217], v[190:193], v[10:13]
	v_mfma_f32_16x16x32_bf16 v[6:9], v[206:209], v[198:201], v[6:9]
	v_mfma_f32_16x16x32_bf16 v[2:5], v[214:217], v[198:201], v[2:5]
	s_add_i32 s59, s59, 2
	s_add_u32 s24, s24, 0x100
	s_addc_u32 s25, s25, 0
	s_add_u32 s57, s57, 0x100
	s_addc_u32 s58, s58, 0
	s_cmp_gt_u32 s59, 29
	s_barrier
	s_cbranch_scc0 .LBB0_85
	v_lshl_add_u32 v1, s10, 8, v147
	v_lshl_or_b32 v154, s54, 8, v149
	v_ashrrev_i32_e32 v155, 31, v154
	v_mov_b64_e32 v[156:157], s[96:97]
	v_cvt_pk_bf16_f32 v70, v70, v71
	v_cvt_pk_bf16_f32 v71, v72, v73
	v_cvt_pk_bf16_f32 v72, v66, v67
	v_add_u32_e32 v66, 0x80, v1
	v_mad_i64_i32 v[158:159], s[24:25], v1, s53, v[156:157]
	v_lshlrev_b64 v[154:155], 1, v[154:155]
	v_cvt_pk_bf16_f32 v110, v110, v111
	v_cvt_pk_bf16_f32 v111, v112, v113
	v_cvt_pk_bf16_f32 v112, v106, v107
	v_or_b32_e32 v106, 16, v1
	v_mad_i64_i32 v[66:67], s[24:25], v66, s53, v[156:157]
	v_cvt_pk_bf16_f32 v46, v46, v47
	v_cvt_pk_bf16_f32 v47, v48, v49
	v_cvt_pk_bf16_f32 v48, v42, v43
	v_add_u32_e32 v42, 0x90, v1
	v_lshl_add_u64 v[158:159], v[158:159], 0, v[154:155]
	v_cvt_pk_bf16_f32 v113, v108, v109
	v_mad_i64_i32 v[106:107], s[24:25], v106, s53, v[156:157]
	v_cvt_pk_bf16_f32 v94, v94, v95
	v_cvt_pk_bf16_f32 v95, v96, v97
	v_cvt_pk_bf16_f32 v96, v90, v91
	v_or_b32_e32 v90, 32, v1
	v_lshl_add_u64 v[66:67], v[66:67], 0, v[154:155]
	v_cvt_pk_bf16_f32 v49, v44, v45
	v_mad_i64_i32 v[42:43], s[24:25], v42, s53, v[156:157]
	v_cvt_pk_bf16_f32 v30, v30, v31
	v_cvt_pk_bf16_f32 v31, v32, v33
	v_cvt_pk_bf16_f32 v32, v26, v27
	v_add_u32_e32 v26, 0xa0, v1
	global_store_dwordx4 v[158:159], v[110:113], off offset:256
	v_cvt_pk_bf16_f32 v97, v92, v93
	v_mad_i64_i32 v[90:91], s[24:25], v90, s53, v[156:157]
	v_lshl_add_u64 v[110:111], v[106:107], 0, v[154:155]
	v_cvt_pk_bf16_f32 v78, v78, v79
	v_cvt_pk_bf16_f32 v79, v80, v81
	v_cvt_pk_bf16_f32 v80, v74, v75
	v_or_b32_e32 v74, 48, v1
	global_store_dwordx4 v[66:67], v[46:49], off offset:256
	v_cvt_pk_bf16_f32 v33, v28, v29
	v_mad_i64_i32 v[26:27], s[24:25], v26, s53, v[156:157]
	v_lshl_add_u64 v[46:47], v[42:43], 0, v[154:155]
	v_add_u32_e32 v1, 0xb0, v1
	global_store_dwordx4 v[110:111], v[94:97], off offset:256
	v_cvt_pk_bf16_f32 v81, v76, v77
	v_mad_i64_i32 v[74:75], s[24:25], v74, s53, v[156:157]
	v_lshl_add_u64 v[94:95], v[90:91], 0, v[154:155]
	global_store_dwordx4 v[46:47], v[30:33], off offset:256
	v_cvt_pk_bf16_f32 v14, v14, v15
	v_cvt_pk_bf16_f32 v15, v16, v17
	v_lshl_add_u64 v[30:31], v[26:27], 0, v[154:155]
	v_cvt_pk_bf16_f32 v16, v10, v11
	v_cvt_pk_bf16_f32 v17, v12, v13
	v_mad_i64_i32 v[10:11], s[24:25], v1, s53, v[156:157]
	v_cvt_pk_bf16_f32 v126, v126, v127
	v_cvt_pk_bf16_f32 v127, v128, v129
	v_cvt_pk_bf16_f32 v128, v122, v123
	v_cvt_pk_bf16_f32 v129, v124, v125
	v_cvt_pk_bf16_f32 v106, v118, v119
	v_cvt_pk_bf16_f32 v107, v120, v121
	v_cvt_pk_bf16_f32 v108, v114, v115
	v_cvt_pk_bf16_f32 v109, v116, v117
	v_cvt_pk_bf16_f32 v90, v102, v103
	v_cvt_pk_bf16_f32 v91, v104, v105
	v_cvt_pk_bf16_f32 v92, v98, v99
	v_cvt_pk_bf16_f32 v93, v100, v101
	global_store_dwordx4 v[94:95], v[78:81], off offset:256
	v_cvt_pk_bf16_f32 v76, v82, v83
	v_cvt_pk_bf16_f32 v77, v84, v85
	v_lshl_add_u64 v[78:79], v[74:75], 0, v[154:155]
	v_cvt_pk_bf16_f32 v74, v86, v87
	v_cvt_pk_bf16_f32 v75, v88, v89
	v_cvt_pk_bf16_f32 v73, v68, v69
	v_cvt_pk_bf16_f32 v62, v62, v63
	v_cvt_pk_bf16_f32 v63, v64, v65
	v_cvt_pk_bf16_f32 v64, v58, v59
	v_cvt_pk_bf16_f32 v65, v60, v61
	v_cvt_pk_bf16_f32 v42, v54, v55
	v_cvt_pk_bf16_f32 v43, v56, v57
	v_cvt_pk_bf16_f32 v44, v50, v51
	v_cvt_pk_bf16_f32 v45, v52, v53
	v_cvt_pk_bf16_f32 v26, v38, v39
	v_cvt_pk_bf16_f32 v27, v40, v41
	v_cvt_pk_bf16_f32 v28, v34, v35
	v_cvt_pk_bf16_f32 v29, v36, v37
	global_store_dwordx4 v[30:31], v[14:17], off offset:256
	v_cvt_pk_bf16_f32 v12, v18, v19
	v_cvt_pk_bf16_f32 v13, v20, v21
	v_lshl_add_u64 v[14:15], v[10:11], 0, v[154:155]
	v_cvt_pk_bf16_f32 v10, v22, v23
	v_cvt_pk_bf16_f32 v11, v24, v25
	v_cvt_pk_bf16_f32 v6, v6, v7
	v_cvt_pk_bf16_f32 v7, v8, v9
	v_cvt_pk_bf16_f32 v8, v2, v3
	v_cvt_pk_bf16_f32 v9, v4, v5
	s_and_b64 vcc, exec, s[0:1]
	s_mov_b32 s54, s12
	s_mov_b32 s10, s14
	s_mov_b64 s[84:85], s[22:23]
	s_mov_b64 s[24:25], s[16:17]
	v_readlane_b32 s93, v254, 9
	global_store_dwordx4 v[158:159], v[126:129], off
	global_store_dwordx4 v[110:111], v[106:109], off
	global_store_dwordx4 v[94:95], v[90:93], off
	global_store_dwordx4 v[78:79], v[74:77], off
	global_store_dwordx4 v[78:79], v[70:73], off offset:256
	global_store_dwordx4 v[66:67], v[62:65], off
	global_store_dwordx4 v[46:47], v[42:45], off
	global_store_dwordx4 v[30:31], v[26:29], off
	global_store_dwordx4 v[14:15], v[10:13], off
	global_store_dwordx4 v[14:15], v[6:9], off offset:256
	s_cbranch_vccz .LBB0_82
	s_waitcnt vmcnt(0)
	s_cmpk_gt_u32 s3, 0xff
	s_cbranch_scc1 .LBB0_89
	s_barrier
